# GDN: the qk tiles (waves 4-7) moved from section c to section d (idle time behind wave 0's forward substitution); section c keeps only the LM tiles on waves 0-3; wave 4 takes no fragment pieces
# baseline (speedup 1.0000x reference)
.Lgpf_done_next:
	s_cmp_lg_u32 s56, 0
	s_cbranch_scc1 .Lgc_join
	v_and_b32_e32 v0, 15, v215
	v_lshrrev_b32_e32 v1, 4, v215
	v_readlane_b32 s0, v253, 51
	v_readlane_b32 s1, v253, 52
	v_add_u32_e32 v2, s9, v0
	v_mul_u32_u24_e32 v3, 0x110, v2
	v_lshl_add_u32 v3, v1, 4, v3
	v_mul_u32_u24_e32 v4, 0x110, v0
	v_lshl_add_u32 v4, v1, 4, v4
	v_add_u32_e32 v3, s0, v3
	v_add_u32_e32 v4, s1, v4
	s_lshl_b32 s20, s9, 2
	s_add_i32 s20, s20, 0x1c400
	v_lshl_add_u32 v5, v1, 4, s20
	v_lshlrev_b32_e32 v6, 2, v0
	v_add_u32_e32 v6, 0x1c400, v6
	ds_read_b128 v[40:43], v3
	ds_read_b128 v[44:47], v3 offset:64
	ds_read_b128 v[48:51], v3 offset:128
	ds_read_b128 v[52:55], v3 offset:192
	s_mov_b32 s34, 0x3fb8aa3b
	s_cmp_eq_u32 s9, 16
	s_cbranch_scc1 .Lgc_v1
	s_cmp_eq_u32 s9, 32
	s_cbranch_scc1 .Lgc_v2
	s_cmp_eq_u32 s9, 48
	s_cbranch_scc1 .Lgc_v3
	s_branch .Lgc_v0

.Lgc_v3:
	ds_read_b128 v[56:59], v4
	ds_read_b128 v[60:63], v4 offset:64
	ds_read_b128 v[64:67], v4 offset:128
	ds_read_b128 v[68:71], v4 offset:192
	ds_read_b128 v[144:147], v5
	ds_read_b32 v136, v6
	ds_read_b32 v137, v6 offset:64
	ds_read_b32 v138, v6 offset:128
	ds_read_b32 v139, v6 offset:192
	ds_read_b128 v[72:75], v4 offset:4352
	ds_read_b128 v[76:79], v4 offset:4416
	ds_read_b128 v[80:83], v4 offset:4480
	ds_read_b128 v[84:87], v4 offset:4544
	ds_read_b128 v[88:91], v4 offset:8704
	ds_read_b128 v[92:95], v4 offset:8768
	ds_read_b128 v[96:99], v4 offset:8832
	ds_read_b128 v[100:103], v4 offset:8896
	ds_read_b128 v[104:107], v4 offset:13056
	ds_read_b128 v[108:111], v4 offset:13120
	ds_read_b128 v[112:115], v4 offset:13184
	ds_read_b128 v[116:119], v4 offset:13248
	v_add_u32_e32 v11, 48, v0
	v_lshl_add_u32 v12, v1, 2, s9
	v_add_u32_e32 v13, 1, v12
	v_add_u32_e32 v14, 2, v12
	v_add_u32_e32 v15, 3, v12
	s_waitcnt lgkmcnt(15)
	v_mfma_f32_16x16x32_bf16 v[120:123], v[40:43], v[56:59], 0
	v_mfma_f32_16x16x32_bf16 v[120:123], v[44:47], v[60:63], v[120:123]
	v_mfma_f32_16x16x32_bf16 v[120:123], v[48:51], v[64:67], v[120:123]
	v_mfma_f32_16x16x32_bf16 v[120:123], v[52:55], v[68:71], v[120:123]
	v_sub_f32_e32 v148, v144, v136
	v_sub_f32_e32 v149, v145, v136
	v_sub_f32_e32 v150, v146, v136
	v_sub_f32_e32 v151, v147, v136
	v_mul_f32_e32 v148, s34, v148
	v_mul_f32_e32 v149, s34, v149
	v_mul_f32_e32 v150, s34, v150
	v_mul_f32_e32 v151, s34, v151
	v_exp_f32_e32 v148, v148
	v_exp_f32_e32 v149, v149
	v_exp_f32_e32 v150, v150
	v_exp_f32_e32 v151, v151
	s_waitcnt lgkmcnt(8)
	v_mfma_f32_16x16x32_bf16 v[124:127], v[40:43], v[72:75], 0
	v_mfma_f32_16x16x32_bf16 v[124:127], v[44:47], v[76:79], v[124:127]
	v_mfma_f32_16x16x32_bf16 v[124:127], v[48:51], v[80:83], v[124:127]
	v_mfma_f32_16x16x32_bf16 v[124:127], v[52:55], v[84:87], v[124:127]
	v_mul_f32_e32 v148, v120, v148
	v_mul_f32_e32 v149, v121, v149
	v_mul_f32_e32 v150, v122, v150
	v_mul_f32_e32 v151, v123, v151
	v_sub_f32_e32 v152, v144, v137
	v_sub_f32_e32 v153, v145, v137
	v_sub_f32_e32 v154, v146, v137
	v_sub_f32_e32 v155, v147, v137
	v_mul_f32_e32 v152, s34, v152
	v_mul_f32_e32 v153, s34, v153
	v_mul_f32_e32 v154, s34, v154
	v_mul_f32_e32 v155, s34, v155
	v_exp_f32_e32 v152, v152
	v_exp_f32_e32 v153, v153
	v_exp_f32_e32 v154, v154
	v_exp_f32_e32 v155, v155
	s_waitcnt lgkmcnt(4)
	v_mfma_f32_16x16x32_bf16 v[128:131], v[40:43], v[88:91], 0
	v_mfma_f32_16x16x32_bf16 v[128:131], v[44:47], v[92:95], v[128:131]
	v_mfma_f32_16x16x32_bf16 v[128:131], v[48:51], v[96:99], v[128:131]
	v_mfma_f32_16x16x32_bf16 v[128:131], v[52:55], v[100:103], v[128:131]
	v_mul_f32_e32 v152, v124, v152
	v_mul_f32_e32 v153, v125, v153
	v_mul_f32_e32 v154, v126, v154
	v_mul_f32_e32 v155, v127, v155
	v_sub_f32_e32 v156, v144, v138
	v_sub_f32_e32 v157, v145, v138
	v_sub_f32_e32 v158, v146, v138
	v_sub_f32_e32 v159, v147, v138
	v_mul_f32_e32 v156, s34, v156
	v_mul_f32_e32 v157, s34, v157
	v_mul_f32_e32 v158, s34, v158
	v_mul_f32_e32 v159, s34, v159
	v_exp_f32_e32 v156, v156
	v_exp_f32_e32 v157, v157
	v_exp_f32_e32 v158, v158
	v_exp_f32_e32 v159, v159
	s_waitcnt lgkmcnt(0)
	v_mfma_f32_16x16x32_bf16 v[132:135], v[40:43], v[104:107], 0
	v_mfma_f32_16x16x32_bf16 v[132:135], v[44:47], v[108:111], v[132:135]
	v_mfma_f32_16x16x32_bf16 v[132:135], v[48:51], v[112:115], v[132:135]
	v_mfma_f32_16x16x32_bf16 v[132:135], v[52:55], v[116:119], v[132:135]
	v_mul_f32_e32 v156, v128, v156
	v_mul_f32_e32 v157, v129, v157
	v_mul_f32_e32 v158, v130, v158
	v_mul_f32_e32 v159, v131, v159
	v_sub_f32_e32 v160, v144, v139
	v_sub_f32_e32 v161, v145, v139
	v_sub_f32_e32 v162, v146, v139
	v_sub_f32_e32 v163, v147, v139
	v_mul_f32_e32 v160, s34, v160
	v_mul_f32_e32 v161, s34, v161
	v_mul_f32_e32 v162, s34, v162
	v_mul_f32_e32 v163, s34, v163
	v_exp_f32_e32 v160, v160
	v_exp_f32_e32 v161, v161
	v_exp_f32_e32 v162, v162
	v_exp_f32_e32 v163, v163
	v_mul_f32_e32 v160, v132, v160
	v_mul_f32_e32 v161, v133, v161
	v_mul_f32_e32 v162, v134, v162
	v_mul_f32_e32 v163, v135, v163
	v_cmp_lt_i32_e32 vcc, v11, v12
	v_cmp_lt_i32_e64 s[0:1], v11, v13
	v_cmp_lt_i32_e64 s[20:21], v11, v14
	v_cndmask_b32_e32 v160, 0, v160, vcc
	v_cmp_lt_i32_e32 vcc, v11, v15
	v_cndmask_b32_e64 v161, 0, v161, s[0:1]
	v_cndmask_b32_e64 v162, 0, v162, s[20:21]
	s_nop 0
	v_cndmask_b32_e32 v163, 0, v163, vcc
	s_branch .Lgc_st
.Lgc_st:
	v_mul_u32_u24_e32 v16, 0x110, v0
	s_lshl_b32 s34, s9, 2
	s_add_i32 s34, s34, 0x15c00
	v_lshl_add_u32 v16, v1, 4, v16
	v_add_u32_e32 v16, s34, v16
	ds_write_b128 v16, v[148:151]
	ds_write_b128 v16, v[152:155] offset:4352
	ds_write_b128 v16, v[156:159] offset:8704
	ds_write_b128 v16, v[160:163] offset:13056
	s_cmp_lt_u32 s9, 32
	s_cbranch_scc1 .Lgc_join
	s_mul_i32 s34, s9, 0x50
	s_add_i32 s34, s34, 0x1be00
	v_mul_u32_u24_e32 v17, 0x140, v1
	v_lshl_add_u32 v17, v0, 1, v17
	v_add_u32_e32 v17, s34, v17
	v_cvt_pk_bf16_f32 v164, v148, v148
	v_cvt_pk_bf16_f32 v165, v149, v149
	v_cvt_pk_bf16_f32 v166, v150, v150
	v_cvt_pk_bf16_f32 v167, v151, v151
	v_cvt_pk_bf16_f32 v168, v152, v152
	v_cvt_pk_bf16_f32 v169, v153, v153
	v_cvt_pk_bf16_f32 v170, v154, v154
	v_cvt_pk_bf16_f32 v171, v155, v155
	ds_write_b16 v17, v164
	ds_write_b16 v17, v165 offset:80
	ds_write_b16 v17, v166 offset:160
	ds_write_b16 v17, v167 offset:240
	ds_write_b16 v17, v168 offset:32
	ds_write_b16 v17, v169 offset:112
	ds_write_b16 v17, v170 offset:192
	ds_write_b16 v17, v171 offset:272
.Lgc_join:
	v_readlane_b32 s82, v253, 17
	v_readlane_b32 s83, v253, 18
	s_not_b64 s[2:3], s[56:57]

.Lgpf_done_nxd:
	s_mov_b64 s[0:1], -1
	s_cmp_lt_u32 s82, 4
	s_cbranch_scc1 .Lgq_skip
	v_and_b32_e32 v0, 15, v215
	v_lshrrev_b32_e32 v1, 4, v215
	v_readlane_b32 s0, v253, 51
	v_readlane_b32 s1, v253, 52
	v_add_u32_e32 v2, s9, v0
	v_mul_u32_u24_e32 v3, 0x110, v2
	v_lshl_add_u32 v3, v1, 4, v3
	v_mul_u32_u24_e32 v4, 0x110, v0
	v_lshl_add_u32 v4, v1, 4, v4
	v_add_u32_e32 v3, s0, v3
	v_add_u32_e32 v4, s1, v4
	s_lshl_b32 s20, s9, 2
	s_add_i32 s20, s20, 0x1c400
	v_lshl_add_u32 v5, v1, 4, s20
	v_lshlrev_b32_e32 v6, 2, v0
	v_add_u32_e32 v6, 0x1c400, v6
	ds_read_b128 v[40:43], v3
	ds_read_b128 v[44:47], v3 offset:64
	ds_read_b128 v[48:51], v3 offset:128
	ds_read_b128 v[52:55], v3 offset:192
	s_mov_b32 s34, 0xbfb8aa3b
	s_cmp_eq_u32 s9, 16
	s_cbranch_scc1 .Lgq_v1
	s_cmp_eq_u32 s9, 32
	s_cbranch_scc1 .Lgq_v2
	s_cmp_eq_u32 s9, 48
	s_cbranch_scc1 .Lgq_v3
	s_branch .Lgq_v0

.Lgq_st:
	s_add_u32 s2, s78, 0xc000
	s_addc_u32 s3, s79, 0
	s_lshl_b32 s34, s9, 6
	v_lshlrev_b32_e32 v16, 4, v0
	v_and_b32_e32 v17, 1, v1
	v_lshl_add_u32 v16, v17, 9, v16
	v_lshrrev_b32_e32 v17, 1, v1
	v_lshl_add_u32 v16, v17, 3, v16
	v_add_u32_e32 v16, s34, v16
	v_add_u32_e32 v17, 0x1000, v16
	v_cvt_pk_bf16_f32 v164, v148, v149
	v_cvt_pk_bf16_f32 v165, v150, v151
	v_cvt_pk_bf16_f32 v166, v152, v153
	v_cvt_pk_bf16_f32 v167, v154, v155
	v_cvt_pk_bf16_f32 v168, v156, v157
	v_cvt_pk_bf16_f32 v169, v158, v159
	v_cvt_pk_bf16_f32 v170, v160, v161
	v_cvt_pk_bf16_f32 v171, v162, v163
	global_store_dwordx2 v16, v[164:165], s[2:3]
	global_store_dwordx2 v16, v[166:167], s[2:3] offset:256
	global_store_dwordx2 v17, v[168:169], s[2:3]
	global_store_dwordx2 v17, v[170:171], s[2:3] offset:256
	s_not_b64 s[2:3], s[56:57]
	s_mov_b64 s[0:1], -1
.Lgq_skip:
	v_and_b32_e32 v0, 31, v215
	v_lshrrev_b32_e32 v1, 5, v215
	v_mul_u32_u24_e32 v2, 0x110, v0
	v_lshl_add_u32 v2, v1, 3, v2
	v_add_u32_e32 v2, 0x8800, v2
	v_lshlrev_b32_e32 v3, 2, v0
	v_add_u32_e32 v3, 0x1c600, v3
	v_mul_u32_u24_e32 v4, 0x440, v1
	v_lshl_add_u32 v4, v0, 1, v4
	v_lshlrev_b32_e32 v5, 4, v1
	v_add_u32_e32 v5, 0x1c700, v5
	v_lshlrev_b32_e32 v6, 4, v215
	s_cmp_eq_u32 s82, 4
	s_cbranch_scc1 .Lgp_pre
	s_cmp_gt_u32 s82, 4
	s_cselect_b32 s35, 2, 1
	s_sub_i32 s34, s82, s35
	s_cmp_gt_u32 s34, 31
	s_cbranch_scc1 .Lgp_rd_done
	s_cmp_gt_u32 s34, 15
	s_cbranch_scc1 .Lgp_rk0
	s_lshr_b32 s20, s34, 3
	s_mul_i32 s21, s20, 0x2200
	s_lshl_b32 s22, s34, 5
	s_and_b32 s22, s22, 0xe0
	s_add_i32 s21, s21, s22
	v_add_u32_e32 v8, s21, v2
	ds_read2_b64 v[16:19], v8 offset1:2
	s_lshl_b32 s20, s20, 7
	v_add_u32_e32 v9, s20, v3
	ds_read_b32 v20, v9
	s_branch .Lgp_rn0

.Lgp_rn0:
	s_add_i32 s34, s34, 6
	s_cmp_gt_u32 s34, 31
	s_cbranch_scc1 .Lgp_rd_done
	s_cmp_gt_u32 s34, 15
	s_cbranch_scc1 .Lgp_rk1
	s_lshr_b32 s20, s34, 3
	s_mul_i32 s21, s20, 0x2200
	s_lshl_b32 s22, s34, 5
	s_and_b32 s22, s22, 0xe0
	s_add_i32 s21, s21, s22
	v_add_u32_e32 v8, s21, v2
	ds_read2_b64 v[36:39], v8 offset1:2
	s_lshl_b32 s20, s20, 7
	v_add_u32_e32 v9, s20, v3
	ds_read_b32 v40, v9
	s_branch .Lgp_rn1

.Lgp_rn1:
	s_add_i32 s34, s34, 6
	s_cmp_gt_u32 s34, 31
	s_cbranch_scc1 .Lgp_rd_done
	s_cmp_gt_u32 s34, 15
	s_cbranch_scc1 .Lgp_rk2
	s_lshr_b32 s20, s34, 3
	s_mul_i32 s21, s20, 0x2200
	s_lshl_b32 s22, s34, 5
	s_and_b32 s22, s22, 0xe0
	s_add_i32 s21, s21, s22
	v_add_u32_e32 v8, s21, v2
	ds_read2_b64 v[56:59], v8 offset1:2
	s_lshl_b32 s20, s20, 7
	v_add_u32_e32 v9, s20, v3
	ds_read_b32 v60, v9
	s_branch .Lgp_rn2

.Lgp_rn2:
	s_add_i32 s34, s34, 6
	s_cmp_gt_u32 s34, 31
	s_cbranch_scc1 .Lgp_rd_done
	s_cmp_gt_u32 s34, 15
	s_cbranch_scc1 .Lgp_rk3
	s_lshr_b32 s20, s34, 3
	s_mul_i32 s21, s20, 0x2200
	s_lshl_b32 s22, s34, 5
	s_and_b32 s22, s22, 0xe0
	s_add_i32 s21, s21, s22
	v_add_u32_e32 v8, s21, v2
	ds_read2_b64 v[76:79], v8 offset1:2
	s_lshl_b32 s20, s20, 7
	v_add_u32_e32 v9, s20, v3
	ds_read_b32 v80, v9
	s_branch .Lgp_rn3

.Lgp_rn3:
	s_add_i32 s34, s34, 6
	s_cmp_gt_u32 s34, 31
	s_cbranch_scc1 .Lgp_rd_done
	s_cmp_gt_u32 s34, 15
	s_cbranch_scc1 .Lgp_rk4
	s_lshr_b32 s20, s34, 3
	s_mul_i32 s21, s20, 0x2200
	s_lshl_b32 s22, s34, 5
	s_and_b32 s22, s22, 0xe0
	s_add_i32 s21, s21, s22
	v_add_u32_e32 v8, s21, v2
	ds_read2_b64 v[96:99], v8 offset1:2
	s_lshl_b32 s20, s20, 7
	v_add_u32_e32 v9, s20, v3
	ds_read_b32 v100, v9
	s_branch .Lgp_rn4

.Lgp_rn4:
	s_add_i32 s34, s34, 6
	s_cmp_gt_u32 s34, 31
	s_cbranch_scc1 .Lgp_rd_done
	s_cmp_gt_u32 s34, 15
	s_cbranch_scc1 .Lgp_rk5
	s_lshr_b32 s20, s34, 3
	s_mul_i32 s21, s20, 0x2200
	s_lshl_b32 s22, s34, 5
	s_and_b32 s22, s22, 0xe0
	s_add_i32 s21, s21, s22
	v_add_u32_e32 v8, s21, v2
	ds_read2_b64 v[116:119], v8 offset1:2
	s_lshl_b32 s20, s20, 7
	v_add_u32_e32 v9, s20, v3
	ds_read_b32 v120, v9
	s_branch .Lgp_rn5
.Lgp_rk5:
	s_and_b32 s20, s34, 3
	s_mul_i32 s21, s20, 0x1100
	s_bfe_u32 s22, s34, 0x20002
	s_lshl_b32 s23, s22, 6
	s_add_i32 s21, s21, s23
	v_add_u32_e32 v8, s21, v4
	ds_read_u16 v116, v8
	ds_read_u16 v117, v8 offset:272
	ds_read_u16 v118, v8 offset:544
	ds_read_u16 v119, v8 offset:816
	ds_read_u16 v120, v8 offset:2176
	ds_read_u16 v121, v8 offset:2448
	ds_read_u16 v122, v8 offset:2720
	ds_read_u16 v123, v8 offset:2992
	s_lshl_b32 s20, s20, 6
	v_add_u32_e32 v9, s20, v5
	ds_read_b128 v[124:127], v9
	ds_read_b128 v[128:131], v9 offset:32
.Lgp_rn5:
.Lgp_rd_done:
	s_waitcnt lgkmcnt(0)
	s_sub_i32 s34, s82, s35
	s_cmp_gt_u32 s34, 31
	s_cbranch_scc1 .Lgp_pre
	s_lshl_b32 s20, s34, 10
	s_add_i32 s20, s20, 0x4000
	v_add_u32_e32 v8, s20, v6
	s_cmp_gt_u32 s34, 15
	s_cbranch_scc1 .Lgp_ck0
	v_lshlrev_b32_e32 v24, 16, v16
	v_and_b32_e32 v25, 0xffff0000, v16
	v_lshlrev_b32_e32 v26, 16, v17
	v_and_b32_e32 v27, 0xffff0000, v17
	v_lshlrev_b32_e32 v28, 16, v18
	v_and_b32_e32 v29, 0xffff0000, v18
	v_lshlrev_b32_e32 v30, 16, v19
	v_and_b32_e32 v31, 0xffff0000, v19
	v_mul_f32_e32 v24, v20, v24
	v_mul_f32_e32 v25, v20, v25
	v_mul_f32_e32 v26, v20, v26
	v_mul_f32_e32 v27, v20, v27
	v_mul_f32_e32 v28, v20, v28
	v_mul_f32_e32 v29, v20, v29
	v_mul_f32_e32 v30, v20, v30
	v_mul_f32_e32 v31, v20, v31
	v_cvt_pk_bf16_f32 v16, v24, v25
	v_cvt_pk_bf16_f32 v17, v26, v27
	v_cvt_pk_bf16_f32 v18, v28, v29
	v_cvt_pk_bf16_f32 v19, v30, v31
	global_store_dwordx4 v8, v[16:19], s[78:79]
	s_branch .Lgp_cn0

.Lgp_cn0:
	s_add_i32 s34, s34, 6
	s_cmp_gt_u32 s34, 31
	s_cbranch_scc1 .Lgp_pre
	s_lshl_b32 s20, s34, 10
	s_add_i32 s20, s20, 0x4000
	v_add_u32_e32 v8, s20, v6
	s_cmp_gt_u32 s34, 15
	s_cbranch_scc1 .Lgp_ck1
	v_lshlrev_b32_e32 v44, 16, v36
	v_and_b32_e32 v45, 0xffff0000, v36
	v_lshlrev_b32_e32 v46, 16, v37
	v_and_b32_e32 v47, 0xffff0000, v37
	v_lshlrev_b32_e32 v48, 16, v38
	v_and_b32_e32 v49, 0xffff0000, v38
	v_lshlrev_b32_e32 v50, 16, v39
	v_and_b32_e32 v51, 0xffff0000, v39
	v_mul_f32_e32 v44, v40, v44
	v_mul_f32_e32 v45, v40, v45
	v_mul_f32_e32 v46, v40, v46
	v_mul_f32_e32 v47, v40, v47
	v_mul_f32_e32 v48, v40, v48
	v_mul_f32_e32 v49, v40, v49
	v_mul_f32_e32 v50, v40, v50
	v_mul_f32_e32 v51, v40, v51
	v_cvt_pk_bf16_f32 v36, v44, v45
	v_cvt_pk_bf16_f32 v37, v46, v47
	v_cvt_pk_bf16_f32 v38, v48, v49
	v_cvt_pk_bf16_f32 v39, v50, v51
	global_store_dwordx4 v8, v[36:39], s[78:79]
	s_branch .Lgp_cn1

.Lgp_cn1:
	s_add_i32 s34, s34, 6
	s_cmp_gt_u32 s34, 31
	s_cbranch_scc1 .Lgp_pre
	s_lshl_b32 s20, s34, 10
	s_add_i32 s20, s20, 0x4000
	v_add_u32_e32 v8, s20, v6
	s_cmp_gt_u32 s34, 15
	s_cbranch_scc1 .Lgp_ck2
	v_lshlrev_b32_e32 v64, 16, v56
	v_and_b32_e32 v65, 0xffff0000, v56
	v_lshlrev_b32_e32 v66, 16, v57
	v_and_b32_e32 v67, 0xffff0000, v57
	v_lshlrev_b32_e32 v68, 16, v58
	v_and_b32_e32 v69, 0xffff0000, v58
	v_lshlrev_b32_e32 v70, 16, v59
	v_and_b32_e32 v71, 0xffff0000, v59
	v_mul_f32_e32 v64, v60, v64
	v_mul_f32_e32 v65, v60, v65
	v_mul_f32_e32 v66, v60, v66
	v_mul_f32_e32 v67, v60, v67
	v_mul_f32_e32 v68, v60, v68
	v_mul_f32_e32 v69, v60, v69
	v_mul_f32_e32 v70, v60, v70
	v_mul_f32_e32 v71, v60, v71
	v_cvt_pk_bf16_f32 v56, v64, v65
	v_cvt_pk_bf16_f32 v57, v66, v67
	v_cvt_pk_bf16_f32 v58, v68, v69
	v_cvt_pk_bf16_f32 v59, v70, v71
	global_store_dwordx4 v8, v[56:59], s[78:79]
	s_branch .Lgp_cn2

.Lgp_cn2:
	s_add_i32 s34, s34, 6
	s_cmp_gt_u32 s34, 31
	s_cbranch_scc1 .Lgp_pre
	s_lshl_b32 s20, s34, 10
	s_add_i32 s20, s20, 0x4000
	v_add_u32_e32 v8, s20, v6
	s_cmp_gt_u32 s34, 15
	s_cbranch_scc1 .Lgp_ck3
	v_lshlrev_b32_e32 v84, 16, v76
	v_and_b32_e32 v85, 0xffff0000, v76
	v_lshlrev_b32_e32 v86, 16, v77
	v_and_b32_e32 v87, 0xffff0000, v77
	v_lshlrev_b32_e32 v88, 16, v78
	v_and_b32_e32 v89, 0xffff0000, v78
	v_lshlrev_b32_e32 v90, 16, v79
	v_and_b32_e32 v91, 0xffff0000, v79
	v_mul_f32_e32 v84, v80, v84
	v_mul_f32_e32 v85, v80, v85
	v_mul_f32_e32 v86, v80, v86
	v_mul_f32_e32 v87, v80, v87
	v_mul_f32_e32 v88, v80, v88
	v_mul_f32_e32 v89, v80, v89
	v_mul_f32_e32 v90, v80, v90
	v_mul_f32_e32 v91, v80, v91
	v_cvt_pk_bf16_f32 v76, v84, v85
	v_cvt_pk_bf16_f32 v77, v86, v87
	v_cvt_pk_bf16_f32 v78, v88, v89
	v_cvt_pk_bf16_f32 v79, v90, v91
	global_store_dwordx4 v8, v[76:79], s[78:79]
	s_branch .Lgp_cn3

.Lgp_cn3:
	s_add_i32 s34, s34, 6
	s_cmp_gt_u32 s34, 31
	s_cbranch_scc1 .Lgp_pre
	s_lshl_b32 s20, s34, 10
	s_add_i32 s20, s20, 0x4000
	v_add_u32_e32 v8, s20, v6
	s_cmp_gt_u32 s34, 15
	s_cbranch_scc1 .Lgp_ck4
	v_lshlrev_b32_e32 v104, 16, v96
	v_and_b32_e32 v105, 0xffff0000, v96
	v_lshlrev_b32_e32 v106, 16, v97
	v_and_b32_e32 v107, 0xffff0000, v97
	v_lshlrev_b32_e32 v108, 16, v98
	v_and_b32_e32 v109, 0xffff0000, v98
	v_lshlrev_b32_e32 v110, 16, v99
	v_and_b32_e32 v111, 0xffff0000, v99
	v_mul_f32_e32 v104, v100, v104
	v_mul_f32_e32 v105, v100, v105
	v_mul_f32_e32 v106, v100, v106
	v_mul_f32_e32 v107, v100, v107
	v_mul_f32_e32 v108, v100, v108
	v_mul_f32_e32 v109, v100, v109
	v_mul_f32_e32 v110, v100, v110
	v_mul_f32_e32 v111, v100, v111
	v_cvt_pk_bf16_f32 v96, v104, v105
	v_cvt_pk_bf16_f32 v97, v106, v107
	v_cvt_pk_bf16_f32 v98, v108, v109
	v_cvt_pk_bf16_f32 v99, v110, v111
	global_store_dwordx4 v8, v[96:99], s[78:79]
	s_branch .Lgp_cn4

.Lgp_cn4:
	s_add_i32 s34, s34, 6
	s_cmp_gt_u32 s34, 31
	s_cbranch_scc1 .Lgp_pre
	s_lshl_b32 s20, s34, 10
	s_add_i32 s20, s20, 0x4000
	v_add_u32_e32 v8, s20, v6
	s_cmp_gt_u32 s34, 15
	s_cbranch_scc1 .Lgp_ck5
	v_lshlrev_b32_e32 v124, 16, v116
	v_and_b32_e32 v125, 0xffff0000, v116
	v_lshlrev_b32_e32 v126, 16, v117
	v_and_b32_e32 v127, 0xffff0000, v117
	v_lshlrev_b32_e32 v128, 16, v118
	v_and_b32_e32 v129, 0xffff0000, v118
	v_lshlrev_b32_e32 v130, 16, v119
	v_and_b32_e32 v131, 0xffff0000, v119
	v_mul_f32_e32 v124, v120, v124
	v_mul_f32_e32 v125, v120, v125
	v_mul_f32_e32 v126, v120, v126
	v_mul_f32_e32 v127, v120, v127
	v_mul_f32_e32 v128, v120, v128
	v_mul_f32_e32 v129, v120, v129
	v_mul_f32_e32 v130, v120, v130
	v_mul_f32_e32 v131, v120, v131
	v_cvt_pk_bf16_f32 v116, v124, v125
	v_cvt_pk_bf16_f32 v117, v126, v127
	v_cvt_pk_bf16_f32 v118, v128, v129
	v_cvt_pk_bf16_f32 v119, v130, v131
	global_store_dwordx4 v8, v[116:119], s[78:79]
	s_branch .Lgp_cn5
.Lgp_ck5:
	v_lshlrev_b32_e32 v116, 16, v116
	v_lshlrev_b32_e32 v117, 16, v117
	v_lshlrev_b32_e32 v118, 16, v118
	v_lshlrev_b32_e32 v119, 16, v119
	v_lshlrev_b32_e32 v120, 16, v120
	v_lshlrev_b32_e32 v121, 16, v121
	v_lshlrev_b32_e32 v122, 16, v122
	v_lshlrev_b32_e32 v123, 16, v123
	v_mul_f32_e32 v116, v124, v116
	v_mul_f32_e32 v117, v125, v117
	v_mul_f32_e32 v118, v126, v118
	v_mul_f32_e32 v119, v127, v119
	v_mul_f32_e32 v120, v128, v120
	v_mul_f32_e32 v121, v129, v121
	v_mul_f32_e32 v122, v130, v122
	v_mul_f32_e32 v123, v131, v123
	v_cvt_pk_bf16_f32 v132, v116, v117
	v_cvt_pk_bf16_f32 v133, v118, v119
	v_cvt_pk_bf16_f32 v134, v120, v121
	v_cvt_pk_bf16_f32 v135, v122, v123
	global_store_dwordx4 v8, v[132:135], s[78:79]
